# attention fast loop unrolled x6 over the 3-slot LDS rings so every LDS offset is an immediate (no per-step ring bookkeeping, no address VALU), on top of the R3 structure and the workgroup-uniform path
# speedup vs baseline: 1.0518x; 1.0518x over previous
.LBB0_1138:
	v_mov_b32_e32 v224, 0
	s_mov_b32 s1, 0
	v_mov_b32_e32 v36, 0
	v_mov_b32_e32 v37, 0
	v_mov_b32_e32 v38, 0
	v_mov_b32_e32 v39, 0
	v_mov_b32_e32 v40, 0
	v_mov_b32_e32 v41, 0
	v_mov_b32_e32 v42, 0
	v_mov_b32_e32 v43, 0
	v_mov_b32_e32 v44, 0
	v_mov_b32_e32 v45, 0
	v_mov_b32_e32 v46, 0
	v_mov_b32_e32 v47, 0
	v_mov_b32_e32 v48, 0
	v_mov_b32_e32 v49, 0
	v_mov_b32_e32 v50, 0
	v_mov_b32_e32 v51, 0
	v_mov_b32_e32 v52, 0
	v_mov_b32_e32 v53, 0
	v_mov_b32_e32 v54, 0
	v_mov_b32_e32 v55, 0
	v_mov_b32_e32 v56, 0
	v_mov_b32_e32 v57, 0
	v_mov_b32_e32 v58, 0
	v_mov_b32_e32 v59, 0
	v_mov_b32_e32 v60, 0
	v_mov_b32_e32 v61, 0
	v_mov_b32_e32 v62, 0
	v_mov_b32_e32 v63, 0
	v_mov_b32_e32 v64, 0
	v_mov_b32_e32 v65, 0
	v_mov_b32_e32 v66, 0
	v_mov_b32_e32 v67, 0
	v_add_u32_e32 v178, v218, v217
	ds_read_b128 v[166:169], v205 offset:13312
	ds_read_b128 v[170:173], v205 offset:19968
	ds_read_b128 v[174:177], v205 offset:13344
	ds_read_b128 v[206:209], v205 offset:20000
	ds_read_b128 v[226:229], v205 offset:13376
	s_add_i32 s2, s23, s1
	s_add_i32 s3, s2, 2
	s_cmp_ge_u32 s2, s34
	s_cselect_b32 s7, s34, 0
	s_sub_i32 s2, s2, s7
	s_cmp_ge_u32 s3, s34
	s_cselect_b32 s7, s34, 0
	s_sub_i32 s3, s3, s7
	s_cmp_ge_u32 s3, s34
	s_cselect_b32 s7, s34, 0
	s_sub_i32 s3, s3, s7
	v_lshl_add_u32 v230, s3, v215, v223
	global_load_dwordx4 v[230:233], v230, s[44:45]
	v_mad_u32_u24 v234, s3, v199, v202
	global_load_dwordx2 v[234:235], v234, s[44:45]
	s_add_i32 s2, s23, s1
	s_add_i32 s3, s2, 3
	s_add_i32 s2, s2, 1
	s_cmp_ge_u32 s2, s34
	s_cselect_b32 s7, s34, 0
	s_sub_i32 s2, s2, s7
	s_cmp_ge_u32 s3, s34
	s_cselect_b32 s7, s34, 0
	s_sub_i32 s3, s3, s7
	s_cmp_ge_u32 s3, s34
	s_cselect_b32 s7, s34, 0
	s_sub_i32 s3, s3, s7
	v_lshl_add_u32 v156, s3, v215, v223
	global_load_dwordx4 v[156:159], v156, s[44:45]
	v_mad_u32_u24 v160, s3, v199, v202
	global_load_dwordx2 v[160:161], v160, s[44:45]
	v_lshl_add_u32 v162, s2, 7, v204
	global_load_dwordx4 v[162:165], v162, s[44:45]
	s_waitcnt lgkmcnt(4)
	v_mfma_f32_32x32x16_bf16 v[84:99], v[166:169], v[132:135], 0
	ds_read_b128 v[166:169], v205 offset:20032
	v_exp_f32_e32 v20, v20
	v_exp_f32_e32 v4, v4
	v_exp_f32_e32 v21, v21
	v_add_f32_e32 v179, v4, v20
	v_exp_f32_e32 v5, v5
	s_waitcnt lgkmcnt(4)
	v_mfma_f32_32x32x16_bf16 v[68:83], v[170:173], v[132:135], 0
	ds_read_b128 v[170:173], v205 offset:13408
	v_add_f32_e32 v179, v21, v179
	v_cvt_pk_bf16_f32 v100, v20, v21
	v_exp_f32_e32 v22, v22
	v_add_f32_e32 v179, v5, v179
	v_exp_f32_e32 v6, v6
	v_add_f32_e32 v179, v22, v179
	v_cvt_pk_bf16_f32 v108, v4, v5
	s_waitcnt lgkmcnt(4)
	v_mfma_f32_32x32x16_bf16 v[84:99], v[174:177], v[136:139], v[84:99]
	ds_read_b128 v[174:177], v205 offset:20064
	v_exp_f32_e32 v23, v23
	v_add_f32_e32 v179, v6, v179
	v_exp_f32_e32 v7, v7
	v_add_f32_e32 v179, v23, v179
	v_cvt_pk_bf16_f32 v101, v22, v23
	v_exp_f32_e32 v24, v24
	v_add_f32_e32 v179, v7, v179
	s_waitcnt lgkmcnt(4)
	v_mfma_f32_32x32x16_bf16 v[68:83], v[206:209], v[136:139], v[68:83]
	ds_read_b128 v[206:209], v205 offset:13440
	v_exp_f32_e32 v8, v8
	v_add_f32_e32 v179, v24, v179
	v_cvt_pk_bf16_f32 v109, v6, v7
	v_exp_f32_e32 v25, v25
	v_add_f32_e32 v179, v8, v179
	v_exp_f32_e32 v9, v9
	s_waitcnt lgkmcnt(4)
	v_mfma_f32_32x32x16_bf16 v[84:99], v[226:229], v[140:143], v[84:99]
	ds_read_b128 v[226:229], v205 offset:20096
	s_waitcnt vmcnt(3)
	ds_write_b128 v219, v[230:233] offset:45056
	ds_write_b64 v220, v[234:235] offset:45056
	v_add_f32_e32 v179, v25, v179
	v_cvt_pk_bf16_f32 v102, v24, v25
	v_exp_f32_e32 v26, v26
	v_add_f32_e32 v179, v9, v179
	v_exp_f32_e32 v10, v10
	v_add_f32_e32 v179, v26, v179
	v_cvt_pk_bf16_f32 v110, v8, v9
	s_waitcnt lgkmcnt(6)
	v_mfma_f32_32x32x16_bf16 v[68:83], v[166:169], v[140:143], v[68:83]
	ds_read_b128 v[166:169], v205 offset:13472
	v_exp_f32_e32 v27, v27
	v_add_f32_e32 v179, v10, v179
	v_exp_f32_e32 v11, v11
	v_add_f32_e32 v179, v27, v179
	v_cvt_pk_bf16_f32 v103, v26, v27
	v_exp_f32_e32 v28, v28
	v_add_f32_e32 v179, v11, v179
	s_waitcnt lgkmcnt(6)
	v_mfma_f32_32x32x16_bf16 v[84:99], v[170:173], v[144:147], v[84:99]
	ds_read_b128 v[170:173], v205 offset:20128
	v_exp_f32_e32 v29, v29
	v_add_f32_e32 v179, v28, v179
	v_cvt_pk_bf16_f32 v111, v10, v11
	v_exp_f32_e32 v30, v30
	v_add_f32_e32 v179, v29, v179
	v_exp_f32_e32 v31, v31
	s_waitcnt lgkmcnt(6)
	v_mfma_f32_32x32x16_bf16 v[68:83], v[174:177], v[144:147], v[68:83]
	v_add_f32_e32 v179, v30, v179
	v_cvt_pk_bf16_f32 v104, v28, v29
	v_exp_f32_e32 v32, v32
	v_add_f32_e32 v179, v31, v179
	v_exp_f32_e32 v33, v33
	v_add_f32_e32 v179, v32, v179
	v_cvt_pk_bf16_f32 v105, v30, v31
	s_waitcnt lgkmcnt(5)
	v_mfma_f32_32x32x16_bf16 v[84:99], v[206:209], v[148:151], v[84:99]
	s_waitcnt vmcnt(0)
	ds_write_b128 v219, v[156:159] offset:0
	ds_write_b64 v220, v[160:161] offset:0
	ds_write_b64 v221, v[162:163] offset:35840
	ds_write_b64 v222, v[164:165] offset:35840
	s_add_i32 s2, s23, s1
	s_add_i32 s3, s2, 4
	s_add_i32 s2, s2, 2
	s_cmp_ge_u32 s2, s34
	s_cselect_b32 s7, s34, 0
	s_sub_i32 s2, s2, s7
	s_cmp_ge_u32 s3, s34
	s_cselect_b32 s7, s34, 0
	s_sub_i32 s3, s3, s7
	s_cmp_ge_u32 s3, s34
	s_cselect_b32 s7, s34, 0
	s_sub_i32 s3, s3, s7
	v_lshl_add_u32 v156, s3, v215, v223
	global_load_dwordx4 v[156:159], v156, s[44:45]
	v_mad_u32_u24 v160, s3, v199, v202
	global_load_dwordx2 v[160:161], v160, s[44:45]
	v_lshl_add_u32 v162, s2, 7, v204
	global_load_dwordx4 v[162:165], v162, s[44:45]
	v_exp_f32_e32 v34, v34
	v_add_f32_e32 v179, v33, v179
	v_exp_f32_e32 v35, v35
	v_add_f32_e32 v179, v34, v179
	v_cvt_pk_bf16_f32 v106, v32, v33
	v_exp_f32_e32 v12, v12
	v_add_f32_e32 v179, v35, v179
	s_waitcnt lgkmcnt(8)
	v_mfma_f32_32x32x16_bf16 v[68:83], v[226:229], v[148:151], v[68:83]
	v_exp_f32_e32 v13, v13
	v_add_f32_e32 v179, v12, v179
	v_cvt_pk_bf16_f32 v107, v34, v35
	v_exp_f32_e32 v14, v14
	v_add_f32_e32 v179, v13, v179
	v_exp_f32_e32 v15, v15
	s_waitcnt lgkmcnt(5)
	v_mfma_f32_32x32x16_bf16 v[84:99], v[166:169], v[152:155], v[84:99]
	v_add_f32_e32 v179, v14, v179
	v_cvt_pk_bf16_f32 v112, v12, v13
	v_exp_f32_e32 v16, v16
	v_add_f32_e32 v179, v15, v179
	v_exp_f32_e32 v17, v17
	v_add_f32_e32 v179, v16, v179
	v_cvt_pk_bf16_f32 v113, v14, v15
	s_waitcnt lgkmcnt(4)
	v_mfma_f32_32x32x16_bf16 v[68:83], v[170:173], v[152:155], v[68:83]
	v_exp_f32_e32 v18, v18
	v_add_f32_e32 v179, v17, v179
	v_exp_f32_e32 v19, v19
	v_add_f32_e32 v179, v18, v179
	v_cvt_pk_bf16_f32 v114, v16, v17
	v_add_f32_e32 v179, v19, v179
	v_cvt_pk_bf16_f32 v115, v18, v19
	v_add_f32_e32 v224, v224, v179
	s_add_i32 s1, s1, 1
	s_waitcnt lgkmcnt(0)
	s_barrier
	ds_read_b128 v[166:169], v205 offset:45056
	ds_read_b128 v[170:173], v205 offset:51712
	ds_read_b128 v[174:177], v205 offset:45088
	ds_read_b128 v[206:209], v205 offset:51744
	ds_read_b128 v[226:229], v205 offset:45120
	s_waitcnt lgkmcnt(0)
.Latt_u6_top:
	s_waitcnt lgkmcnt(4)
	v_mfma_f32_32x32x16_bf16 v[20:35], v[166:169], v[132:135], 0
	ds_read_b128 v[166:169], v205 offset:51776
	v_exp_f32_e32 v84, v84
	v_exp_f32_e32 v68, v68
	v_exp_f32_e32 v85, v85
	s_waitcnt lgkmcnt(4)
	v_mfma_f32_32x32x16_bf16 v[4:19], v[170:173], v[132:135], 0
	ds_read_b128 v[170:173], v205 offset:45152
	v_add_f32_e32 v179, v68, v84
	v_exp_f32_e32 v69, v69
	v_add_f32_e32 v179, v85, v179
	v_cvt_pk_bf16_f32 v116, v84, v85
	s_waitcnt lgkmcnt(4)
	v_mfma_f32_32x32x16_bf16 v[20:35], v[174:177], v[136:139], v[20:35]
	ds_read_b128 v[174:177], v205 offset:51808
	v_exp_f32_e32 v86, v86
	v_add_f32_e32 v179, v69, v179
	v_exp_f32_e32 v70, v70
	v_add_f32_e32 v179, v86, v179
	s_waitcnt lgkmcnt(4)
	v_mfma_f32_32x32x16_bf16 v[4:19], v[206:209], v[136:139], v[4:19]
	ds_read_b128 v[206:209], v205 offset:45184
	v_cvt_pk_bf16_f32 v124, v68, v69
	v_exp_f32_e32 v87, v87
	v_add_f32_e32 v179, v70, v179
	v_exp_f32_e32 v71, v71
	s_waitcnt lgkmcnt(4)
	v_mfma_f32_32x32x16_bf16 v[20:35], v[226:229], v[140:143], v[20:35]
	ds_read_b128 v[226:229], v205 offset:51840
	v_add_f32_e32 v179, v87, v179
	v_cvt_pk_bf16_f32 v117, v86, v87
	v_exp_f32_e32 v88, v88
	v_add_f32_e32 v179, v71, v179
	s_waitcnt lgkmcnt(4)
	v_mfma_f32_32x32x16_bf16 v[4:19], v[166:169], v[140:143], v[4:19]
	ds_read_b128 v[166:169], v205 offset:45216
	v_exp_f32_e32 v72, v72
	v_add_f32_e32 v179, v88, v179
	v_cvt_pk_bf16_f32 v125, v70, v71
	v_exp_f32_e32 v89, v89
	s_waitcnt lgkmcnt(4)
	v_mfma_f32_32x32x16_bf16 v[20:35], v[170:173], v[144:147], v[20:35]
	ds_read_b128 v[170:173], v205 offset:51872
	v_add_f32_e32 v179, v72, v179
	v_exp_f32_e32 v73, v73
	v_add_f32_e32 v179, v89, v179
	v_cvt_pk_bf16_f32 v118, v88, v89
	s_waitcnt lgkmcnt(4)
	v_mfma_f32_32x32x16_bf16 v[4:19], v[174:177], v[144:147], v[4:19]
	ds_read_b128 v[174:177], v178 offset:26624
	v_exp_f32_e32 v90, v90
	v_add_f32_e32 v179, v73, v179
	v_exp_f32_e32 v74, v74
	v_add_f32_e32 v179, v90, v179
	s_waitcnt lgkmcnt(4)
	v_mfma_f32_32x32x16_bf16 v[20:35], v[206:209], v[148:151], v[20:35]
	ds_read_b128 v[206:209], v178 offset:31232
	v_cvt_pk_bf16_f32 v126, v72, v73
	v_exp_f32_e32 v91, v91
	v_add_f32_e32 v179, v74, v179
	v_exp_f32_e32 v75, v75
	s_waitcnt lgkmcnt(4)
	v_mfma_f32_32x32x16_bf16 v[4:19], v[226:229], v[148:151], v[4:19]
	ds_read_b128 v[226:229], v178 offset:26656
	v_add_f32_e32 v179, v91, v179
	v_cvt_pk_bf16_f32 v119, v90, v91
	v_exp_f32_e32 v92, v92
	v_add_f32_e32 v179, v75, v179
	s_waitcnt lgkmcnt(4)
	v_mfma_f32_32x32x16_bf16 v[20:35], v[166:169], v[152:155], v[20:35]
	ds_read_b128 v[166:169], v178 offset:31264
	v_exp_f32_e32 v93, v93
	v_add_f32_e32 v179, v92, v179
	v_cvt_pk_bf16_f32 v127, v74, v75
	v_exp_f32_e32 v94, v94
	s_waitcnt lgkmcnt(4)
	v_mfma_f32_32x32x16_bf16 v[4:19], v[170:173], v[152:155], v[4:19]
	ds_read_b128 v[170:173], v178 offset:26688
	v_add_f32_e32 v179, v93, v179
	v_exp_f32_e32 v95, v95
	v_add_f32_e32 v179, v94, v179
	v_cvt_pk_bf16_f32 v120, v92, v93
	s_waitcnt lgkmcnt(4)
	v_mfma_f32_32x32x16_bf16 v[36:51], v[174:177], v[100:103], v[36:51]
	ds_read_b128 v[174:177], v178 offset:31296
	s_waitcnt vmcnt(0)
	ds_write_b128 v219, v[156:159] offset:13312
	ds_write_b64 v220, v[160:161] offset:13312
	ds_write_b64 v221, v[162:163] offset:58368
	ds_write_b64 v222, v[164:165] offset:58368
	s_add_i32 s2, s23, s1
	s_add_i32 s3, s2, 4
	s_add_i32 s2, s2, 2
	s_cmp_ge_u32 s2, s34
	s_cselect_b32 s7, s34, 0
	s_sub_i32 s2, s2, s7
	s_cmp_ge_u32 s3, s34
	s_cselect_b32 s7, s34, 0
	s_sub_i32 s3, s3, s7
	s_cmp_ge_u32 s3, s34
	s_cselect_b32 s7, s34, 0
	s_sub_i32 s3, s3, s7
	v_lshl_add_u32 v156, s3, v215, v223
	global_load_dwordx4 v[156:159], v156, s[44:45]
	v_mad_u32_u24 v160, s3, v199, v202
	global_load_dwordx2 v[160:161], v160, s[44:45]
	v_lshl_add_u32 v162, s2, 7, v204
	global_load_dwordx4 v[162:165], v162, s[44:45]
	v_exp_f32_e32 v96, v96
	v_add_f32_e32 v179, v95, v179
	v_exp_f32_e32 v97, v97
	v_add_f32_e32 v179, v96, v179
	s_waitcnt lgkmcnt(8)
	v_mfma_f32_32x32x16_bf16 v[52:67], v[206:209], v[100:103], v[52:67]
	ds_read_b128 v[206:209], v178 offset:26720
	v_cvt_pk_bf16_f32 v121, v94, v95
	v_exp_f32_e32 v98, v98
	v_add_f32_e32 v179, v97, v179
	v_exp_f32_e32 v99, v99
	s_waitcnt lgkmcnt(8)
	v_mfma_f32_32x32x16_bf16 v[36:51], v[226:229], v[104:107], v[36:51]
	ds_read_b128 v[226:229], v178 offset:31328
	v_add_f32_e32 v179, v98, v179
	v_cvt_pk_bf16_f32 v122, v96, v97
	v_exp_f32_e32 v76, v76
	v_add_f32_e32 v179, v99, v179
	s_waitcnt lgkmcnt(8)
	v_mfma_f32_32x32x16_bf16 v[52:67], v[166:169], v[104:107], v[52:67]
	ds_read_b128 v[166:169], v205
	v_exp_f32_e32 v77, v77
	v_add_f32_e32 v179, v76, v179
	v_cvt_pk_bf16_f32 v123, v98, v99
	v_exp_f32_e32 v78, v78
	s_waitcnt lgkmcnt(8)
	v_mfma_f32_32x32x16_bf16 v[36:51], v[170:173], v[108:111], v[36:51]
	ds_read_b128 v[170:173], v205 offset:6656
	v_add_f32_e32 v179, v77, v179
	v_exp_f32_e32 v79, v79
	v_add_f32_e32 v179, v78, v179
	v_cvt_pk_bf16_f32 v128, v76, v77
	s_waitcnt lgkmcnt(8)
	v_mfma_f32_32x32x16_bf16 v[52:67], v[174:177], v[108:111], v[52:67]
	ds_read_b128 v[174:177], v205 offset:32
	v_exp_f32_e32 v80, v80
	v_add_f32_e32 v179, v79, v179
	v_exp_f32_e32 v81, v81
	v_add_f32_e32 v179, v80, v179
	s_waitcnt lgkmcnt(4)
	v_mfma_f32_32x32x16_bf16 v[36:51], v[206:209], v[112:115], v[36:51]
	ds_read_b128 v[206:209], v205 offset:6688
	v_cvt_pk_bf16_f32 v129, v78, v79
	v_exp_f32_e32 v82, v82
	v_add_f32_e32 v179, v81, v179
	v_exp_f32_e32 v83, v83
	s_waitcnt lgkmcnt(4)
	v_mfma_f32_32x32x16_bf16 v[52:67], v[226:229], v[112:115], v[52:67]
	ds_read_b128 v[226:229], v205 offset:64
	v_add_f32_e32 v179, v82, v179
	v_cvt_pk_bf16_f32 v130, v80, v81
	v_add_f32_e32 v179, v83, v179
	v_cvt_pk_bf16_f32 v131, v82, v83
	v_add_f32_e32 v224, v224, v179
	s_add_i32 s1, s1, 1
	s_cmp_lt_u32 s1, s34
	s_barrier
	s_cbranch_scc0 .Latt_u6_fin1
	s_waitcnt lgkmcnt(4)
	v_mfma_f32_32x32x16_bf16 v[84:99], v[166:169], v[132:135], 0
	ds_read_b128 v[166:169], v205 offset:6720
	v_exp_f32_e32 v20, v20
	v_exp_f32_e32 v4, v4
	v_exp_f32_e32 v21, v21
	s_waitcnt lgkmcnt(4)
	v_mfma_f32_32x32x16_bf16 v[68:83], v[170:173], v[132:135], 0
	ds_read_b128 v[170:173], v205 offset:96
	v_add_f32_e32 v179, v4, v20
	v_exp_f32_e32 v5, v5
	v_add_f32_e32 v179, v21, v179
	v_cvt_pk_bf16_f32 v100, v20, v21
	s_waitcnt lgkmcnt(4)
	v_mfma_f32_32x32x16_bf16 v[84:99], v[174:177], v[136:139], v[84:99]
	ds_read_b128 v[174:177], v205 offset:6752
	v_exp_f32_e32 v22, v22
	v_add_f32_e32 v179, v5, v179
	v_exp_f32_e32 v6, v6
	v_add_f32_e32 v179, v22, v179
	s_waitcnt lgkmcnt(4)
	v_mfma_f32_32x32x16_bf16 v[68:83], v[206:209], v[136:139], v[68:83]
	ds_read_b128 v[206:209], v205 offset:128
	v_cvt_pk_bf16_f32 v108, v4, v5
	v_exp_f32_e32 v23, v23
	v_add_f32_e32 v179, v6, v179
	v_exp_f32_e32 v7, v7
	s_waitcnt lgkmcnt(4)
	v_mfma_f32_32x32x16_bf16 v[84:99], v[226:229], v[140:143], v[84:99]
	ds_read_b128 v[226:229], v205 offset:6784
	v_add_f32_e32 v179, v23, v179
	v_cvt_pk_bf16_f32 v101, v22, v23
	v_exp_f32_e32 v24, v24
	v_add_f32_e32 v179, v7, v179
	s_waitcnt lgkmcnt(4)
	v_mfma_f32_32x32x16_bf16 v[68:83], v[166:169], v[140:143], v[68:83]
	ds_read_b128 v[166:169], v205 offset:160
	v_exp_f32_e32 v8, v8
	v_add_f32_e32 v179, v24, v179
	v_cvt_pk_bf16_f32 v109, v6, v7
	v_exp_f32_e32 v25, v25
	s_waitcnt lgkmcnt(4)
	v_mfma_f32_32x32x16_bf16 v[84:99], v[170:173], v[144:147], v[84:99]
	ds_read_b128 v[170:173], v205 offset:6816
	v_add_f32_e32 v179, v8, v179
	v_exp_f32_e32 v9, v9
	v_add_f32_e32 v179, v25, v179
	v_cvt_pk_bf16_f32 v102, v24, v25
	s_waitcnt lgkmcnt(4)
	v_mfma_f32_32x32x16_bf16 v[68:83], v[174:177], v[144:147], v[68:83]
	ds_read_b128 v[174:177], v178 offset:35840
	v_exp_f32_e32 v26, v26
	v_add_f32_e32 v179, v9, v179
	v_exp_f32_e32 v10, v10
	v_add_f32_e32 v179, v26, v179
	s_waitcnt lgkmcnt(4)
	v_mfma_f32_32x32x16_bf16 v[84:99], v[206:209], v[148:151], v[84:99]
	ds_read_b128 v[206:209], v178 offset:40448
	v_cvt_pk_bf16_f32 v110, v8, v9
	v_exp_f32_e32 v27, v27
	v_add_f32_e32 v179, v10, v179
	v_exp_f32_e32 v11, v11
	s_waitcnt lgkmcnt(4)
	v_mfma_f32_32x32x16_bf16 v[68:83], v[226:229], v[148:151], v[68:83]
	ds_read_b128 v[226:229], v178 offset:35872
	v_add_f32_e32 v179, v27, v179
	v_cvt_pk_bf16_f32 v103, v26, v27
	v_exp_f32_e32 v28, v28
	v_add_f32_e32 v179, v11, v179
	s_waitcnt lgkmcnt(4)
	v_mfma_f32_32x32x16_bf16 v[84:99], v[166:169], v[152:155], v[84:99]
	ds_read_b128 v[166:169], v178 offset:40480
	v_exp_f32_e32 v29, v29
	v_add_f32_e32 v179, v28, v179
	v_cvt_pk_bf16_f32 v111, v10, v11
	v_exp_f32_e32 v30, v30
	s_waitcnt lgkmcnt(4)
	v_mfma_f32_32x32x16_bf16 v[68:83], v[170:173], v[152:155], v[68:83]
	ds_read_b128 v[170:173], v178 offset:35904
	v_add_f32_e32 v179, v29, v179
	v_exp_f32_e32 v31, v31
	v_add_f32_e32 v179, v30, v179
	v_cvt_pk_bf16_f32 v104, v28, v29
	s_waitcnt lgkmcnt(4)
	v_mfma_f32_32x32x16_bf16 v[36:51], v[174:177], v[116:119], v[36:51]
	ds_read_b128 v[174:177], v178 offset:40512
	s_waitcnt vmcnt(0)
	ds_write_b128 v219, v[156:159] offset:45056
	ds_write_b64 v220, v[160:161] offset:45056
	ds_write_b64 v221, v[162:163] offset:26624
	ds_write_b64 v222, v[164:165] offset:26624
	s_add_i32 s2, s23, s1
	s_add_i32 s3, s2, 4
	s_add_i32 s2, s2, 2
	s_cmp_ge_u32 s2, s34
	s_cselect_b32 s7, s34, 0
	s_sub_i32 s2, s2, s7
	s_cmp_ge_u32 s3, s34
	s_cselect_b32 s7, s34, 0
	s_sub_i32 s3, s3, s7
	s_cmp_ge_u32 s3, s34
	s_cselect_b32 s7, s34, 0
	s_sub_i32 s3, s3, s7
	v_lshl_add_u32 v156, s3, v215, v223
	global_load_dwordx4 v[156:159], v156, s[44:45]
	v_mad_u32_u24 v160, s3, v199, v202
	global_load_dwordx2 v[160:161], v160, s[44:45]
	v_lshl_add_u32 v162, s2, 7, v204
	global_load_dwordx4 v[162:165], v162, s[44:45]
	v_exp_f32_e32 v32, v32
	v_add_f32_e32 v179, v31, v179
	v_exp_f32_e32 v33, v33
	v_add_f32_e32 v179, v32, v179
	s_waitcnt lgkmcnt(8)
	v_mfma_f32_32x32x16_bf16 v[52:67], v[206:209], v[116:119], v[52:67]
	ds_read_b128 v[206:209], v178 offset:35936
	v_cvt_pk_bf16_f32 v105, v30, v31
	v_exp_f32_e32 v34, v34
	v_add_f32_e32 v179, v33, v179
	v_exp_f32_e32 v35, v35
	s_waitcnt lgkmcnt(8)
	v_mfma_f32_32x32x16_bf16 v[36:51], v[226:229], v[120:123], v[36:51]
	ds_read_b128 v[226:229], v178 offset:40544
	v_add_f32_e32 v179, v34, v179
	v_cvt_pk_bf16_f32 v106, v32, v33
	v_exp_f32_e32 v12, v12
	v_add_f32_e32 v179, v35, v179
	s_waitcnt lgkmcnt(8)
	v_mfma_f32_32x32x16_bf16 v[52:67], v[166:169], v[120:123], v[52:67]
	ds_read_b128 v[166:169], v205 offset:13312
	v_exp_f32_e32 v13, v13
	v_add_f32_e32 v179, v12, v179
	v_cvt_pk_bf16_f32 v107, v34, v35
	v_exp_f32_e32 v14, v14
	s_waitcnt lgkmcnt(8)
	v_mfma_f32_32x32x16_bf16 v[36:51], v[170:173], v[124:127], v[36:51]
	ds_read_b128 v[170:173], v205 offset:19968
	v_add_f32_e32 v179, v13, v179
	v_exp_f32_e32 v15, v15
	v_add_f32_e32 v179, v14, v179
	v_cvt_pk_bf16_f32 v112, v12, v13
	s_waitcnt lgkmcnt(8)
	v_mfma_f32_32x32x16_bf16 v[52:67], v[174:177], v[124:127], v[52:67]
	ds_read_b128 v[174:177], v205 offset:13344
	v_exp_f32_e32 v16, v16
	v_add_f32_e32 v179, v15, v179
	v_exp_f32_e32 v17, v17
	v_add_f32_e32 v179, v16, v179
	s_waitcnt lgkmcnt(4)
	v_mfma_f32_32x32x16_bf16 v[36:51], v[206:209], v[128:131], v[36:51]
	ds_read_b128 v[206:209], v205 offset:20000
	v_cvt_pk_bf16_f32 v113, v14, v15
	v_exp_f32_e32 v18, v18
	v_add_f32_e32 v179, v17, v179
	v_exp_f32_e32 v19, v19
	s_waitcnt lgkmcnt(4)
	v_mfma_f32_32x32x16_bf16 v[52:67], v[226:229], v[128:131], v[52:67]
	ds_read_b128 v[226:229], v205 offset:13376
	v_add_f32_e32 v179, v18, v179
	v_cvt_pk_bf16_f32 v114, v16, v17
	v_add_f32_e32 v179, v19, v179
	v_cvt_pk_bf16_f32 v115, v18, v19
	v_add_f32_e32 v224, v224, v179
	s_add_i32 s1, s1, 1
	s_barrier
	s_waitcnt lgkmcnt(4)
	v_mfma_f32_32x32x16_bf16 v[20:35], v[166:169], v[132:135], 0
	ds_read_b128 v[166:169], v205 offset:20032
	v_exp_f32_e32 v84, v84
	v_exp_f32_e32 v68, v68
	v_exp_f32_e32 v85, v85
	s_waitcnt lgkmcnt(4)
	v_mfma_f32_32x32x16_bf16 v[4:19], v[170:173], v[132:135], 0
	ds_read_b128 v[170:173], v205 offset:13408
	v_add_f32_e32 v179, v68, v84
	v_exp_f32_e32 v69, v69
	v_add_f32_e32 v179, v85, v179
	v_cvt_pk_bf16_f32 v116, v84, v85
	s_waitcnt lgkmcnt(4)
	v_mfma_f32_32x32x16_bf16 v[20:35], v[174:177], v[136:139], v[20:35]
	ds_read_b128 v[174:177], v205 offset:20064
	v_exp_f32_e32 v86, v86
	v_add_f32_e32 v179, v69, v179
	v_exp_f32_e32 v70, v70
	v_add_f32_e32 v179, v86, v179
	s_waitcnt lgkmcnt(4)
	v_mfma_f32_32x32x16_bf16 v[4:19], v[206:209], v[136:139], v[4:19]
	ds_read_b128 v[206:209], v205 offset:13440
	v_cvt_pk_bf16_f32 v124, v68, v69
	v_exp_f32_e32 v87, v87
	v_add_f32_e32 v179, v70, v179
	v_exp_f32_e32 v71, v71
	s_waitcnt lgkmcnt(4)
	v_mfma_f32_32x32x16_bf16 v[20:35], v[226:229], v[140:143], v[20:35]
	ds_read_b128 v[226:229], v205 offset:20096
	v_add_f32_e32 v179, v87, v179
	v_cvt_pk_bf16_f32 v117, v86, v87
	v_exp_f32_e32 v88, v88
	v_add_f32_e32 v179, v71, v179
	s_waitcnt lgkmcnt(4)
	v_mfma_f32_32x32x16_bf16 v[4:19], v[166:169], v[140:143], v[4:19]
	ds_read_b128 v[166:169], v205 offset:13472
	v_exp_f32_e32 v72, v72
	v_add_f32_e32 v179, v88, v179
	v_cvt_pk_bf16_f32 v125, v70, v71
	v_exp_f32_e32 v89, v89
	s_waitcnt lgkmcnt(4)
	v_mfma_f32_32x32x16_bf16 v[20:35], v[170:173], v[144:147], v[20:35]
	ds_read_b128 v[170:173], v205 offset:20128
	v_add_f32_e32 v179, v72, v179
	v_exp_f32_e32 v73, v73
	v_add_f32_e32 v179, v89, v179
	v_cvt_pk_bf16_f32 v118, v88, v89
	s_waitcnt lgkmcnt(4)
	v_mfma_f32_32x32x16_bf16 v[4:19], v[174:177], v[144:147], v[4:19]
	ds_read_b128 v[174:177], v178 offset:58368
	v_exp_f32_e32 v90, v90
	v_add_f32_e32 v179, v73, v179
	v_exp_f32_e32 v74, v74
	v_add_f32_e32 v179, v90, v179
	s_waitcnt lgkmcnt(4)
	v_mfma_f32_32x32x16_bf16 v[20:35], v[206:209], v[148:151], v[20:35]
	ds_read_b128 v[206:209], v178 offset:62976
	v_cvt_pk_bf16_f32 v126, v72, v73
	v_exp_f32_e32 v91, v91
	v_add_f32_e32 v179, v74, v179
	v_exp_f32_e32 v75, v75
	s_waitcnt lgkmcnt(4)
	v_mfma_f32_32x32x16_bf16 v[4:19], v[226:229], v[148:151], v[4:19]
	ds_read_b128 v[226:229], v178 offset:58400
	v_add_f32_e32 v179, v91, v179
	v_cvt_pk_bf16_f32 v119, v90, v91
	v_exp_f32_e32 v92, v92
	v_add_f32_e32 v179, v75, v179
	s_waitcnt lgkmcnt(4)
	v_mfma_f32_32x32x16_bf16 v[20:35], v[166:169], v[152:155], v[20:35]
	ds_read_b128 v[166:169], v178 offset:63008
	v_exp_f32_e32 v93, v93
	v_add_f32_e32 v179, v92, v179
	v_cvt_pk_bf16_f32 v127, v74, v75
	v_exp_f32_e32 v94, v94
	s_waitcnt lgkmcnt(4)
	v_mfma_f32_32x32x16_bf16 v[4:19], v[170:173], v[152:155], v[4:19]
	ds_read_b128 v[170:173], v178 offset:58432
	v_add_f32_e32 v179, v93, v179
	v_exp_f32_e32 v95, v95
	v_add_f32_e32 v179, v94, v179
	v_cvt_pk_bf16_f32 v120, v92, v93
	s_waitcnt lgkmcnt(4)
	v_mfma_f32_32x32x16_bf16 v[36:51], v[174:177], v[100:103], v[36:51]
	ds_read_b128 v[174:177], v178 offset:63040
	s_waitcnt vmcnt(0)
	ds_write_b128 v219, v[156:159] offset:0
	ds_write_b64 v220, v[160:161] offset:0
	ds_write_b64 v221, v[162:163] offset:35840
	ds_write_b64 v222, v[164:165] offset:35840
	s_add_i32 s2, s23, s1
	s_add_i32 s3, s2, 4
	s_add_i32 s2, s2, 2
	s_cmp_ge_u32 s2, s34
	s_cselect_b32 s7, s34, 0
	s_sub_i32 s2, s2, s7
	s_cmp_ge_u32 s3, s34
	s_cselect_b32 s7, s34, 0
	s_sub_i32 s3, s3, s7
	s_cmp_ge_u32 s3, s34
	s_cselect_b32 s7, s34, 0
	s_sub_i32 s3, s3, s7
	v_lshl_add_u32 v156, s3, v215, v223
	global_load_dwordx4 v[156:159], v156, s[44:45]
	v_mad_u32_u24 v160, s3, v199, v202
	global_load_dwordx2 v[160:161], v160, s[44:45]
	v_lshl_add_u32 v162, s2, 7, v204
	global_load_dwordx4 v[162:165], v162, s[44:45]
	v_exp_f32_e32 v96, v96
	v_add_f32_e32 v179, v95, v179
	v_exp_f32_e32 v97, v97
	v_add_f32_e32 v179, v96, v179
	s_waitcnt lgkmcnt(8)
	v_mfma_f32_32x32x16_bf16 v[52:67], v[206:209], v[100:103], v[52:67]
	ds_read_b128 v[206:209], v178 offset:58464
	v_cvt_pk_bf16_f32 v121, v94, v95
	v_exp_f32_e32 v98, v98
	v_add_f32_e32 v179, v97, v179
	v_exp_f32_e32 v99, v99
	s_waitcnt lgkmcnt(8)
	v_mfma_f32_32x32x16_bf16 v[36:51], v[226:229], v[104:107], v[36:51]
	ds_read_b128 v[226:229], v178 offset:63072
	v_add_f32_e32 v179, v98, v179
	v_cvt_pk_bf16_f32 v122, v96, v97
	v_exp_f32_e32 v76, v76
	v_add_f32_e32 v179, v99, v179
	s_waitcnt lgkmcnt(8)
	v_mfma_f32_32x32x16_bf16 v[52:67], v[166:169], v[104:107], v[52:67]
	ds_read_b128 v[166:169], v205 offset:45056
	v_exp_f32_e32 v77, v77
	v_add_f32_e32 v179, v76, v179
	v_cvt_pk_bf16_f32 v123, v98, v99
	v_exp_f32_e32 v78, v78
	s_waitcnt lgkmcnt(8)
	v_mfma_f32_32x32x16_bf16 v[36:51], v[170:173], v[108:111], v[36:51]
	ds_read_b128 v[170:173], v205 offset:51712
	v_add_f32_e32 v179, v77, v179
	v_exp_f32_e32 v79, v79
	v_add_f32_e32 v179, v78, v179
	v_cvt_pk_bf16_f32 v128, v76, v77
	s_waitcnt lgkmcnt(8)
	v_mfma_f32_32x32x16_bf16 v[52:67], v[174:177], v[108:111], v[52:67]
	ds_read_b128 v[174:177], v205 offset:45088
	v_exp_f32_e32 v80, v80
	v_add_f32_e32 v179, v79, v179
	v_exp_f32_e32 v81, v81
	v_add_f32_e32 v179, v80, v179
	s_waitcnt lgkmcnt(4)
	v_mfma_f32_32x32x16_bf16 v[36:51], v[206:209], v[112:115], v[36:51]
	ds_read_b128 v[206:209], v205 offset:51744
	v_cvt_pk_bf16_f32 v129, v78, v79
	v_exp_f32_e32 v82, v82
	v_add_f32_e32 v179, v81, v179
	v_exp_f32_e32 v83, v83
	s_waitcnt lgkmcnt(4)
	v_mfma_f32_32x32x16_bf16 v[52:67], v[226:229], v[112:115], v[52:67]
	ds_read_b128 v[226:229], v205 offset:45120
	v_add_f32_e32 v179, v82, v179
	v_cvt_pk_bf16_f32 v130, v80, v81
	v_add_f32_e32 v179, v83, v179
	v_cvt_pk_bf16_f32 v131, v82, v83
	v_add_f32_e32 v224, v224, v179
	s_add_i32 s1, s1, 1
	s_cmp_lt_u32 s1, s34
	s_barrier
	s_cbranch_scc0 .Latt_u6_fin0
	s_waitcnt lgkmcnt(4)
	v_mfma_f32_32x32x16_bf16 v[84:99], v[166:169], v[132:135], 0
	ds_read_b128 v[166:169], v205 offset:51776
	v_exp_f32_e32 v20, v20
	v_exp_f32_e32 v4, v4
	v_exp_f32_e32 v21, v21
	s_waitcnt lgkmcnt(4)
	v_mfma_f32_32x32x16_bf16 v[68:83], v[170:173], v[132:135], 0
	ds_read_b128 v[170:173], v205 offset:45152
	v_add_f32_e32 v179, v4, v20
	v_exp_f32_e32 v5, v5
	v_add_f32_e32 v179, v21, v179
	v_cvt_pk_bf16_f32 v100, v20, v21
	s_waitcnt lgkmcnt(4)
	v_mfma_f32_32x32x16_bf16 v[84:99], v[174:177], v[136:139], v[84:99]
	ds_read_b128 v[174:177], v205 offset:51808
	v_exp_f32_e32 v22, v22
	v_add_f32_e32 v179, v5, v179
	v_exp_f32_e32 v6, v6
	v_add_f32_e32 v179, v22, v179
	s_waitcnt lgkmcnt(4)
	v_mfma_f32_32x32x16_bf16 v[68:83], v[206:209], v[136:139], v[68:83]
	ds_read_b128 v[206:209], v205 offset:45184
	v_cvt_pk_bf16_f32 v108, v4, v5
	v_exp_f32_e32 v23, v23
	v_add_f32_e32 v179, v6, v179
	v_exp_f32_e32 v7, v7
	s_waitcnt lgkmcnt(4)
	v_mfma_f32_32x32x16_bf16 v[84:99], v[226:229], v[140:143], v[84:99]
	ds_read_b128 v[226:229], v205 offset:51840
	v_add_f32_e32 v179, v23, v179
	v_cvt_pk_bf16_f32 v101, v22, v23
	v_exp_f32_e32 v24, v24
	v_add_f32_e32 v179, v7, v179
	s_waitcnt lgkmcnt(4)
	v_mfma_f32_32x32x16_bf16 v[68:83], v[166:169], v[140:143], v[68:83]
	ds_read_b128 v[166:169], v205 offset:45216
	v_exp_f32_e32 v8, v8
	v_add_f32_e32 v179, v24, v179
	v_cvt_pk_bf16_f32 v109, v6, v7
	v_exp_f32_e32 v25, v25
	s_waitcnt lgkmcnt(4)
	v_mfma_f32_32x32x16_bf16 v[84:99], v[170:173], v[144:147], v[84:99]
	ds_read_b128 v[170:173], v205 offset:51872
	v_add_f32_e32 v179, v8, v179
	v_exp_f32_e32 v9, v9
	v_add_f32_e32 v179, v25, v179
	v_cvt_pk_bf16_f32 v102, v24, v25
	s_waitcnt lgkmcnt(4)
	v_mfma_f32_32x32x16_bf16 v[68:83], v[174:177], v[144:147], v[68:83]
	ds_read_b128 v[174:177], v178 offset:26624
	v_exp_f32_e32 v26, v26
	v_add_f32_e32 v179, v9, v179
	v_exp_f32_e32 v10, v10
	v_add_f32_e32 v179, v26, v179
	s_waitcnt lgkmcnt(4)
	v_mfma_f32_32x32x16_bf16 v[84:99], v[206:209], v[148:151], v[84:99]
	ds_read_b128 v[206:209], v178 offset:31232
	v_cvt_pk_bf16_f32 v110, v8, v9
	v_exp_f32_e32 v27, v27
	v_add_f32_e32 v179, v10, v179
	v_exp_f32_e32 v11, v11
	s_waitcnt lgkmcnt(4)
	v_mfma_f32_32x32x16_bf16 v[68:83], v[226:229], v[148:151], v[68:83]
	ds_read_b128 v[226:229], v178 offset:26656
	v_add_f32_e32 v179, v27, v179
	v_cvt_pk_bf16_f32 v103, v26, v27
	v_exp_f32_e32 v28, v28
	v_add_f32_e32 v179, v11, v179
	s_waitcnt lgkmcnt(4)
	v_mfma_f32_32x32x16_bf16 v[84:99], v[166:169], v[152:155], v[84:99]
	ds_read_b128 v[166:169], v178 offset:31264
	v_exp_f32_e32 v29, v29
	v_add_f32_e32 v179, v28, v179
	v_cvt_pk_bf16_f32 v111, v10, v11
	v_exp_f32_e32 v30, v30
	s_waitcnt lgkmcnt(4)
	v_mfma_f32_32x32x16_bf16 v[68:83], v[170:173], v[152:155], v[68:83]
	ds_read_b128 v[170:173], v178 offset:26688
	v_add_f32_e32 v179, v29, v179
	v_exp_f32_e32 v31, v31
	v_add_f32_e32 v179, v30, v179
	v_cvt_pk_bf16_f32 v104, v28, v29
	s_waitcnt lgkmcnt(4)
	v_mfma_f32_32x32x16_bf16 v[36:51], v[174:177], v[116:119], v[36:51]
	ds_read_b128 v[174:177], v178 offset:31296
	s_waitcnt vmcnt(0)
	ds_write_b128 v219, v[156:159] offset:13312
	ds_write_b64 v220, v[160:161] offset:13312
	ds_write_b64 v221, v[162:163] offset:58368
	ds_write_b64 v222, v[164:165] offset:58368
	s_add_i32 s2, s23, s1
	s_add_i32 s3, s2, 4
	s_add_i32 s2, s2, 2
	s_cmp_ge_u32 s2, s34
	s_cselect_b32 s7, s34, 0
	s_sub_i32 s2, s2, s7
	s_cmp_ge_u32 s3, s34
	s_cselect_b32 s7, s34, 0
	s_sub_i32 s3, s3, s7
	s_cmp_ge_u32 s3, s34
	s_cselect_b32 s7, s34, 0
	s_sub_i32 s3, s3, s7
	v_lshl_add_u32 v156, s3, v215, v223
	global_load_dwordx4 v[156:159], v156, s[44:45]
	v_mad_u32_u24 v160, s3, v199, v202
	global_load_dwordx2 v[160:161], v160, s[44:45]
	v_lshl_add_u32 v162, s2, 7, v204
	global_load_dwordx4 v[162:165], v162, s[44:45]
	v_exp_f32_e32 v32, v32
	v_add_f32_e32 v179, v31, v179
	v_exp_f32_e32 v33, v33
	v_add_f32_e32 v179, v32, v179
	s_waitcnt lgkmcnt(8)
	v_mfma_f32_32x32x16_bf16 v[52:67], v[206:209], v[116:119], v[52:67]
	ds_read_b128 v[206:209], v178 offset:26720
	v_cvt_pk_bf16_f32 v105, v30, v31
	v_exp_f32_e32 v34, v34
	v_add_f32_e32 v179, v33, v179
	v_exp_f32_e32 v35, v35
	s_waitcnt lgkmcnt(8)
	v_mfma_f32_32x32x16_bf16 v[36:51], v[226:229], v[120:123], v[36:51]
	ds_read_b128 v[226:229], v178 offset:31328
	v_add_f32_e32 v179, v34, v179
	v_cvt_pk_bf16_f32 v106, v32, v33
	v_exp_f32_e32 v12, v12
	v_add_f32_e32 v179, v35, v179
	s_waitcnt lgkmcnt(8)
	v_mfma_f32_32x32x16_bf16 v[52:67], v[166:169], v[120:123], v[52:67]
	ds_read_b128 v[166:169], v205
	v_exp_f32_e32 v13, v13
	v_add_f32_e32 v179, v12, v179
	v_cvt_pk_bf16_f32 v107, v34, v35
	v_exp_f32_e32 v14, v14
	s_waitcnt lgkmcnt(8)
	v_mfma_f32_32x32x16_bf16 v[36:51], v[170:173], v[124:127], v[36:51]
	ds_read_b128 v[170:173], v205 offset:6656
	v_add_f32_e32 v179, v13, v179
	v_exp_f32_e32 v15, v15
	v_add_f32_e32 v179, v14, v179
	v_cvt_pk_bf16_f32 v112, v12, v13
	s_waitcnt lgkmcnt(8)
	v_mfma_f32_32x32x16_bf16 v[52:67], v[174:177], v[124:127], v[52:67]
	ds_read_b128 v[174:177], v205 offset:32
	v_exp_f32_e32 v16, v16
	v_add_f32_e32 v179, v15, v179
	v_exp_f32_e32 v17, v17
	v_add_f32_e32 v179, v16, v179
	s_waitcnt lgkmcnt(4)
	v_mfma_f32_32x32x16_bf16 v[36:51], v[206:209], v[128:131], v[36:51]
	ds_read_b128 v[206:209], v205 offset:6688
	v_cvt_pk_bf16_f32 v113, v14, v15
	v_exp_f32_e32 v18, v18
	v_add_f32_e32 v179, v17, v179
	v_exp_f32_e32 v19, v19
	s_waitcnt lgkmcnt(4)
	v_mfma_f32_32x32x16_bf16 v[52:67], v[226:229], v[128:131], v[52:67]
	ds_read_b128 v[226:229], v205 offset:64
	v_add_f32_e32 v179, v18, v179
	v_cvt_pk_bf16_f32 v114, v16, v17
	v_add_f32_e32 v179, v19, v179
	v_cvt_pk_bf16_f32 v115, v18, v19
	v_add_f32_e32 v224, v224, v179
	s_add_i32 s1, s1, 1
	s_barrier
	s_waitcnt lgkmcnt(4)
	v_mfma_f32_32x32x16_bf16 v[20:35], v[166:169], v[132:135], 0
	ds_read_b128 v[166:169], v205 offset:6720
	v_exp_f32_e32 v84, v84
	v_exp_f32_e32 v68, v68
	v_exp_f32_e32 v85, v85
	s_waitcnt lgkmcnt(4)
	v_mfma_f32_32x32x16_bf16 v[4:19], v[170:173], v[132:135], 0
	ds_read_b128 v[170:173], v205 offset:96
	v_add_f32_e32 v179, v68, v84
	v_exp_f32_e32 v69, v69
	v_add_f32_e32 v179, v85, v179
	v_cvt_pk_bf16_f32 v116, v84, v85
	s_waitcnt lgkmcnt(4)
	v_mfma_f32_32x32x16_bf16 v[20:35], v[174:177], v[136:139], v[20:35]
	ds_read_b128 v[174:177], v205 offset:6752
	v_exp_f32_e32 v86, v86
	v_add_f32_e32 v179, v69, v179
	v_exp_f32_e32 v70, v70
	v_add_f32_e32 v179, v86, v179
	s_waitcnt lgkmcnt(4)
	v_mfma_f32_32x32x16_bf16 v[4:19], v[206:209], v[136:139], v[4:19]
	ds_read_b128 v[206:209], v205 offset:128
	v_cvt_pk_bf16_f32 v124, v68, v69
	v_exp_f32_e32 v87, v87
	v_add_f32_e32 v179, v70, v179
	v_exp_f32_e32 v71, v71
	s_waitcnt lgkmcnt(4)
	v_mfma_f32_32x32x16_bf16 v[20:35], v[226:229], v[140:143], v[20:35]
	ds_read_b128 v[226:229], v205 offset:6784
	v_add_f32_e32 v179, v87, v179
	v_cvt_pk_bf16_f32 v117, v86, v87
	v_exp_f32_e32 v88, v88
	v_add_f32_e32 v179, v71, v179
	s_waitcnt lgkmcnt(4)
	v_mfma_f32_32x32x16_bf16 v[4:19], v[166:169], v[140:143], v[4:19]
	ds_read_b128 v[166:169], v205 offset:160
	v_exp_f32_e32 v72, v72
	v_add_f32_e32 v179, v88, v179
	v_cvt_pk_bf16_f32 v125, v70, v71
	v_exp_f32_e32 v89, v89
	s_waitcnt lgkmcnt(4)
	v_mfma_f32_32x32x16_bf16 v[20:35], v[170:173], v[144:147], v[20:35]
	ds_read_b128 v[170:173], v205 offset:6816
	v_add_f32_e32 v179, v72, v179
	v_exp_f32_e32 v73, v73
	v_add_f32_e32 v179, v89, v179
	v_cvt_pk_bf16_f32 v118, v88, v89
	s_waitcnt lgkmcnt(4)
	v_mfma_f32_32x32x16_bf16 v[4:19], v[174:177], v[144:147], v[4:19]
	ds_read_b128 v[174:177], v178 offset:35840
	v_exp_f32_e32 v90, v90
	v_add_f32_e32 v179, v73, v179
	v_exp_f32_e32 v74, v74
	v_add_f32_e32 v179, v90, v179
	s_waitcnt lgkmcnt(4)
	v_mfma_f32_32x32x16_bf16 v[20:35], v[206:209], v[148:151], v[20:35]
	ds_read_b128 v[206:209], v178 offset:40448
	v_cvt_pk_bf16_f32 v126, v72, v73
	v_exp_f32_e32 v91, v91
	v_add_f32_e32 v179, v74, v179
	v_exp_f32_e32 v75, v75
	s_waitcnt lgkmcnt(4)
	v_mfma_f32_32x32x16_bf16 v[4:19], v[226:229], v[148:151], v[4:19]
	ds_read_b128 v[226:229], v178 offset:35872
	v_add_f32_e32 v179, v91, v179
	v_cvt_pk_bf16_f32 v119, v90, v91
	v_exp_f32_e32 v92, v92
	v_add_f32_e32 v179, v75, v179
	s_waitcnt lgkmcnt(4)
	v_mfma_f32_32x32x16_bf16 v[20:35], v[166:169], v[152:155], v[20:35]
	ds_read_b128 v[166:169], v178 offset:40480
	v_exp_f32_e32 v93, v93
	v_add_f32_e32 v179, v92, v179
	v_cvt_pk_bf16_f32 v127, v74, v75
	v_exp_f32_e32 v94, v94
	s_waitcnt lgkmcnt(4)
	v_mfma_f32_32x32x16_bf16 v[4:19], v[170:173], v[152:155], v[4:19]
	ds_read_b128 v[170:173], v178 offset:35904
	v_add_f32_e32 v179, v93, v179
	v_exp_f32_e32 v95, v95
	v_add_f32_e32 v179, v94, v179
	v_cvt_pk_bf16_f32 v120, v92, v93
	s_waitcnt lgkmcnt(4)
	v_mfma_f32_32x32x16_bf16 v[36:51], v[174:177], v[100:103], v[36:51]
	ds_read_b128 v[174:177], v178 offset:40512
	s_waitcnt vmcnt(0)
	ds_write_b128 v219, v[156:159] offset:45056
	ds_write_b64 v220, v[160:161] offset:45056
	ds_write_b64 v221, v[162:163] offset:26624
	ds_write_b64 v222, v[164:165] offset:26624
	s_add_i32 s2, s23, s1
	s_add_i32 s3, s2, 4
	s_add_i32 s2, s2, 2
	s_cmp_ge_u32 s2, s34
	s_cselect_b32 s7, s34, 0
	s_sub_i32 s2, s2, s7
	s_cmp_ge_u32 s3, s34
	s_cselect_b32 s7, s34, 0
	s_sub_i32 s3, s3, s7
	s_cmp_ge_u32 s3, s34
	s_cselect_b32 s7, s34, 0
	s_sub_i32 s3, s3, s7
	v_lshl_add_u32 v156, s3, v215, v223
	global_load_dwordx4 v[156:159], v156, s[44:45]
	v_mad_u32_u24 v160, s3, v199, v202
	global_load_dwordx2 v[160:161], v160, s[44:45]
	v_lshl_add_u32 v162, s2, 7, v204
	global_load_dwordx4 v[162:165], v162, s[44:45]
	v_exp_f32_e32 v96, v96
	v_add_f32_e32 v179, v95, v179
	v_exp_f32_e32 v97, v97
	v_add_f32_e32 v179, v96, v179
	s_waitcnt lgkmcnt(8)
	v_mfma_f32_32x32x16_bf16 v[52:67], v[206:209], v[100:103], v[52:67]
	ds_read_b128 v[206:209], v178 offset:35936
	v_cvt_pk_bf16_f32 v121, v94, v95
	v_exp_f32_e32 v98, v98
	v_add_f32_e32 v179, v97, v179
	v_exp_f32_e32 v99, v99
	s_waitcnt lgkmcnt(8)
	v_mfma_f32_32x32x16_bf16 v[36:51], v[226:229], v[104:107], v[36:51]
	ds_read_b128 v[226:229], v178 offset:40544
	v_add_f32_e32 v179, v98, v179
	v_cvt_pk_bf16_f32 v122, v96, v97
	v_exp_f32_e32 v76, v76
	v_add_f32_e32 v179, v99, v179
	s_waitcnt lgkmcnt(8)
	v_mfma_f32_32x32x16_bf16 v[52:67], v[166:169], v[104:107], v[52:67]
	ds_read_b128 v[166:169], v205 offset:13312
	v_exp_f32_e32 v77, v77
	v_add_f32_e32 v179, v76, v179
	v_cvt_pk_bf16_f32 v123, v98, v99
	v_exp_f32_e32 v78, v78
	s_waitcnt lgkmcnt(8)
	v_mfma_f32_32x32x16_bf16 v[36:51], v[170:173], v[108:111], v[36:51]
	ds_read_b128 v[170:173], v205 offset:19968
	v_add_f32_e32 v179, v77, v179
	v_exp_f32_e32 v79, v79
	v_add_f32_e32 v179, v78, v179
	v_cvt_pk_bf16_f32 v128, v76, v77
	s_waitcnt lgkmcnt(8)
	v_mfma_f32_32x32x16_bf16 v[52:67], v[174:177], v[108:111], v[52:67]
	ds_read_b128 v[174:177], v205 offset:13344
	v_exp_f32_e32 v80, v80
	v_add_f32_e32 v179, v79, v179
	v_exp_f32_e32 v81, v81
	v_add_f32_e32 v179, v80, v179
	s_waitcnt lgkmcnt(4)
	v_mfma_f32_32x32x16_bf16 v[36:51], v[206:209], v[112:115], v[36:51]
	ds_read_b128 v[206:209], v205 offset:20000
	v_cvt_pk_bf16_f32 v129, v78, v79
	v_exp_f32_e32 v82, v82
	v_add_f32_e32 v179, v81, v179
	v_exp_f32_e32 v83, v83
	s_waitcnt lgkmcnt(4)
	v_mfma_f32_32x32x16_bf16 v[52:67], v[226:229], v[112:115], v[52:67]
	ds_read_b128 v[226:229], v205 offset:13376
	v_add_f32_e32 v179, v82, v179
	v_cvt_pk_bf16_f32 v130, v80, v81
	v_add_f32_e32 v179, v83, v179
	v_cvt_pk_bf16_f32 v131, v82, v83
	v_add_f32_e32 v224, v224, v179
	s_add_i32 s1, s1, 1
	s_cmp_lt_u32 s1, s34
	s_barrier
	s_cbranch_scc0 .Latt_u6_fin2
	s_waitcnt lgkmcnt(4)
	v_mfma_f32_32x32x16_bf16 v[84:99], v[166:169], v[132:135], 0
	ds_read_b128 v[166:169], v205 offset:20032
	v_exp_f32_e32 v20, v20
	v_exp_f32_e32 v4, v4
	v_exp_f32_e32 v21, v21
	s_waitcnt lgkmcnt(4)
	v_mfma_f32_32x32x16_bf16 v[68:83], v[170:173], v[132:135], 0
	ds_read_b128 v[170:173], v205 offset:13408
	v_add_f32_e32 v179, v4, v20
	v_exp_f32_e32 v5, v5
	v_add_f32_e32 v179, v21, v179
	v_cvt_pk_bf16_f32 v100, v20, v21
	s_waitcnt lgkmcnt(4)
	v_mfma_f32_32x32x16_bf16 v[84:99], v[174:177], v[136:139], v[84:99]
	ds_read_b128 v[174:177], v205 offset:20064
	v_exp_f32_e32 v22, v22
	v_add_f32_e32 v179, v5, v179
	v_exp_f32_e32 v6, v6
	v_add_f32_e32 v179, v22, v179
	s_waitcnt lgkmcnt(4)
	v_mfma_f32_32x32x16_bf16 v[68:83], v[206:209], v[136:139], v[68:83]
	ds_read_b128 v[206:209], v205 offset:13440
	v_cvt_pk_bf16_f32 v108, v4, v5
	v_exp_f32_e32 v23, v23
	v_add_f32_e32 v179, v6, v179
	v_exp_f32_e32 v7, v7
	s_waitcnt lgkmcnt(4)
	v_mfma_f32_32x32x16_bf16 v[84:99], v[226:229], v[140:143], v[84:99]
	ds_read_b128 v[226:229], v205 offset:20096
	v_add_f32_e32 v179, v23, v179
	v_cvt_pk_bf16_f32 v101, v22, v23
	v_exp_f32_e32 v24, v24
	v_add_f32_e32 v179, v7, v179
	s_waitcnt lgkmcnt(4)
	v_mfma_f32_32x32x16_bf16 v[68:83], v[166:169], v[140:143], v[68:83]
	ds_read_b128 v[166:169], v205 offset:13472
	v_exp_f32_e32 v8, v8
	v_add_f32_e32 v179, v24, v179
	v_cvt_pk_bf16_f32 v109, v6, v7
	v_exp_f32_e32 v25, v25
	s_waitcnt lgkmcnt(4)
	v_mfma_f32_32x32x16_bf16 v[84:99], v[170:173], v[144:147], v[84:99]
	ds_read_b128 v[170:173], v205 offset:20128
	v_add_f32_e32 v179, v8, v179
	v_exp_f32_e32 v9, v9
	v_add_f32_e32 v179, v25, v179
	v_cvt_pk_bf16_f32 v102, v24, v25
	s_waitcnt lgkmcnt(4)
	v_mfma_f32_32x32x16_bf16 v[68:83], v[174:177], v[144:147], v[68:83]
	ds_read_b128 v[174:177], v178 offset:58368
	v_exp_f32_e32 v26, v26
	v_add_f32_e32 v179, v9, v179
	v_exp_f32_e32 v10, v10
	v_add_f32_e32 v179, v26, v179
	s_waitcnt lgkmcnt(4)
	v_mfma_f32_32x32x16_bf16 v[84:99], v[206:209], v[148:151], v[84:99]
	ds_read_b128 v[206:209], v178 offset:62976
	v_cvt_pk_bf16_f32 v110, v8, v9
	v_exp_f32_e32 v27, v27
	v_add_f32_e32 v179, v10, v179
	v_exp_f32_e32 v11, v11
	s_waitcnt lgkmcnt(4)
	v_mfma_f32_32x32x16_bf16 v[68:83], v[226:229], v[148:151], v[68:83]
	ds_read_b128 v[226:229], v178 offset:58400
	v_add_f32_e32 v179, v27, v179
	v_cvt_pk_bf16_f32 v103, v26, v27
	v_exp_f32_e32 v28, v28
	v_add_f32_e32 v179, v11, v179
	s_waitcnt lgkmcnt(4)
	v_mfma_f32_32x32x16_bf16 v[84:99], v[166:169], v[152:155], v[84:99]
	ds_read_b128 v[166:169], v178 offset:63008
	v_exp_f32_e32 v29, v29
	v_add_f32_e32 v179, v28, v179
	v_cvt_pk_bf16_f32 v111, v10, v11
	v_exp_f32_e32 v30, v30
	s_waitcnt lgkmcnt(4)
	v_mfma_f32_32x32x16_bf16 v[68:83], v[170:173], v[152:155], v[68:83]
	ds_read_b128 v[170:173], v178 offset:58432
	v_add_f32_e32 v179, v29, v179
	v_exp_f32_e32 v31, v31
	v_add_f32_e32 v179, v30, v179
	v_cvt_pk_bf16_f32 v104, v28, v29
	s_waitcnt lgkmcnt(4)
	v_mfma_f32_32x32x16_bf16 v[36:51], v[174:177], v[116:119], v[36:51]
	ds_read_b128 v[174:177], v178 offset:63040
	s_waitcnt vmcnt(0)
	ds_write_b128 v219, v[156:159] offset:0
	ds_write_b64 v220, v[160:161] offset:0
	ds_write_b64 v221, v[162:163] offset:35840
	ds_write_b64 v222, v[164:165] offset:35840
	s_add_i32 s2, s23, s1
	s_add_i32 s3, s2, 4
	s_add_i32 s2, s2, 2
	s_cmp_ge_u32 s2, s34
	s_cselect_b32 s7, s34, 0
	s_sub_i32 s2, s2, s7
	s_cmp_ge_u32 s3, s34
	s_cselect_b32 s7, s34, 0
	s_sub_i32 s3, s3, s7
	s_cmp_ge_u32 s3, s34
	s_cselect_b32 s7, s34, 0
	s_sub_i32 s3, s3, s7
	v_lshl_add_u32 v156, s3, v215, v223
	global_load_dwordx4 v[156:159], v156, s[44:45]
	v_mad_u32_u24 v160, s3, v199, v202
	global_load_dwordx2 v[160:161], v160, s[44:45]
	v_lshl_add_u32 v162, s2, 7, v204
	global_load_dwordx4 v[162:165], v162, s[44:45]
	v_exp_f32_e32 v32, v32
	v_add_f32_e32 v179, v31, v179
	v_exp_f32_e32 v33, v33
	v_add_f32_e32 v179, v32, v179
	s_waitcnt lgkmcnt(8)
	v_mfma_f32_32x32x16_bf16 v[52:67], v[206:209], v[116:119], v[52:67]
	ds_read_b128 v[206:209], v178 offset:58464
	v_cvt_pk_bf16_f32 v105, v30, v31
	v_exp_f32_e32 v34, v34
	v_add_f32_e32 v179, v33, v179
	v_exp_f32_e32 v35, v35
	s_waitcnt lgkmcnt(8)
	v_mfma_f32_32x32x16_bf16 v[36:51], v[226:229], v[120:123], v[36:51]
	ds_read_b128 v[226:229], v178 offset:63072
	v_add_f32_e32 v179, v34, v179
	v_cvt_pk_bf16_f32 v106, v32, v33
	v_exp_f32_e32 v12, v12
	v_add_f32_e32 v179, v35, v179
	s_waitcnt lgkmcnt(8)
	v_mfma_f32_32x32x16_bf16 v[52:67], v[166:169], v[120:123], v[52:67]
	ds_read_b128 v[166:169], v205 offset:45056
	v_exp_f32_e32 v13, v13
	v_add_f32_e32 v179, v12, v179
	v_cvt_pk_bf16_f32 v107, v34, v35
	v_exp_f32_e32 v14, v14
	s_waitcnt lgkmcnt(8)
	v_mfma_f32_32x32x16_bf16 v[36:51], v[170:173], v[124:127], v[36:51]
	ds_read_b128 v[170:173], v205 offset:51712
	v_add_f32_e32 v179, v13, v179
	v_exp_f32_e32 v15, v15
	v_add_f32_e32 v179, v14, v179
	v_cvt_pk_bf16_f32 v112, v12, v13
	s_waitcnt lgkmcnt(8)
	v_mfma_f32_32x32x16_bf16 v[52:67], v[174:177], v[124:127], v[52:67]
	ds_read_b128 v[174:177], v205 offset:45088
	v_exp_f32_e32 v16, v16
	v_add_f32_e32 v179, v15, v179
	v_exp_f32_e32 v17, v17
	v_add_f32_e32 v179, v16, v179
	s_waitcnt lgkmcnt(4)
	v_mfma_f32_32x32x16_bf16 v[36:51], v[206:209], v[128:131], v[36:51]
	ds_read_b128 v[206:209], v205 offset:51744
	v_cvt_pk_bf16_f32 v113, v14, v15
	v_exp_f32_e32 v18, v18
	v_add_f32_e32 v179, v17, v179
	v_exp_f32_e32 v19, v19
	s_waitcnt lgkmcnt(4)
	v_mfma_f32_32x32x16_bf16 v[52:67], v[226:229], v[128:131], v[52:67]
	ds_read_b128 v[226:229], v205 offset:45120
	v_add_f32_e32 v179, v18, v179
	v_cvt_pk_bf16_f32 v114, v16, v17
	v_add_f32_e32 v179, v19, v179
	v_cvt_pk_bf16_f32 v115, v18, v19
	v_add_f32_e32 v224, v224, v179
	s_add_i32 s1, s1, 1
	s_barrier
	s_branch .Latt_u6_top
.Latt_u6_fin0:
	ds_read_b128 v[166:169], v178 offset:26624
	ds_read_b128 v[170:173], v178 offset:31232
	ds_read_b128 v[174:177], v178 offset:26656
	ds_read_b128 v[206:209], v178 offset:31264
	ds_read_b128 v[226:229], v178 offset:26688
	s_waitcnt lgkmcnt(4)
	v_mfma_f32_32x32x16_bf16 v[36:51], v[166:169], v[116:119], v[36:51]
	ds_read_b128 v[166:169], v178 offset:31296
	s_waitcnt lgkmcnt(4)
	v_mfma_f32_32x32x16_bf16 v[52:67], v[170:173], v[116:119], v[52:67]
	ds_read_b128 v[170:173], v178 offset:26720
	s_waitcnt lgkmcnt(4)
	v_mfma_f32_32x32x16_bf16 v[36:51], v[174:177], v[120:123], v[36:51]
	ds_read_b128 v[174:177], v178 offset:31328
	s_waitcnt lgkmcnt(4)
	v_mfma_f32_32x32x16_bf16 v[52:67], v[206:209], v[120:123], v[52:67]
	s_waitcnt lgkmcnt(3)
	v_mfma_f32_32x32x16_bf16 v[36:51], v[226:229], v[124:127], v[36:51]
	s_waitcnt lgkmcnt(2)
	v_mfma_f32_32x32x16_bf16 v[52:67], v[166:169], v[124:127], v[52:67]
	s_waitcnt lgkmcnt(1)
	v_mfma_f32_32x32x16_bf16 v[36:51], v[170:173], v[128:131], v[36:51]
	s_waitcnt lgkmcnt(0)
	v_mfma_f32_32x32x16_bf16 v[52:67], v[174:177], v[128:131], v[52:67]
	s_waitcnt vmcnt(0)
	s_branch .LBB0_1109
.Latt_u6_fin1:
	ds_read_b128 v[166:169], v178 offset:35840
	ds_read_b128 v[170:173], v178 offset:40448
	ds_read_b128 v[174:177], v178 offset:35872
	ds_read_b128 v[206:209], v178 offset:40480
	ds_read_b128 v[226:229], v178 offset:35904
	s_waitcnt lgkmcnt(4)
	v_mfma_f32_32x32x16_bf16 v[36:51], v[166:169], v[116:119], v[36:51]
	ds_read_b128 v[166:169], v178 offset:40512
	s_waitcnt lgkmcnt(4)
	v_mfma_f32_32x32x16_bf16 v[52:67], v[170:173], v[116:119], v[52:67]
	ds_read_b128 v[170:173], v178 offset:35936
	s_waitcnt lgkmcnt(4)
	v_mfma_f32_32x32x16_bf16 v[36:51], v[174:177], v[120:123], v[36:51]
	ds_read_b128 v[174:177], v178 offset:40544
	s_waitcnt lgkmcnt(4)
	v_mfma_f32_32x32x16_bf16 v[52:67], v[206:209], v[120:123], v[52:67]
	s_waitcnt lgkmcnt(3)
	v_mfma_f32_32x32x16_bf16 v[36:51], v[226:229], v[124:127], v[36:51]
	s_waitcnt lgkmcnt(2)
	v_mfma_f32_32x32x16_bf16 v[52:67], v[166:169], v[124:127], v[52:67]
	s_waitcnt lgkmcnt(1)
	v_mfma_f32_32x32x16_bf16 v[36:51], v[170:173], v[128:131], v[36:51]
	s_waitcnt lgkmcnt(0)
	v_mfma_f32_32x32x16_bf16 v[52:67], v[174:177], v[128:131], v[52:67]
	s_waitcnt vmcnt(0)
	s_branch .LBB0_1109
.Latt_u6_fin2:
	ds_read_b128 v[166:169], v178 offset:58368
	ds_read_b128 v[170:173], v178 offset:62976
	ds_read_b128 v[174:177], v178 offset:58400
	ds_read_b128 v[206:209], v178 offset:63008
	ds_read_b128 v[226:229], v178 offset:58432
	s_waitcnt lgkmcnt(4)
	v_mfma_f32_32x32x16_bf16 v[36:51], v[166:169], v[116:119], v[36:51]
	ds_read_b128 v[166:169], v178 offset:63040
	s_waitcnt lgkmcnt(4)
	v_mfma_f32_32x32x16_bf16 v[52:67], v[170:173], v[116:119], v[52:67]
	ds_read_b128 v[170:173], v178 offset:58464
	s_waitcnt lgkmcnt(4)
	v_mfma_f32_32x32x16_bf16 v[36:51], v[174:177], v[120:123], v[36:51]
	ds_read_b128 v[174:177], v178 offset:63072
	s_waitcnt lgkmcnt(4)
	v_mfma_f32_32x32x16_bf16 v[52:67], v[206:209], v[120:123], v[52:67]
	s_waitcnt lgkmcnt(3)
	v_mfma_f32_32x32x16_bf16 v[36:51], v[226:229], v[124:127], v[36:51]
	s_waitcnt lgkmcnt(2)
	v_mfma_f32_32x32x16_bf16 v[52:67], v[166:169], v[124:127], v[52:67]
	s_waitcnt lgkmcnt(1)
	v_mfma_f32_32x32x16_bf16 v[36:51], v[170:173], v[128:131], v[36:51]
	s_waitcnt lgkmcnt(0)
	v_mfma_f32_32x32x16_bf16 v[52:67], v[174:177], v[128:131], v[52:67]
	s_waitcnt vmcnt(0)
	s_branch .LBB0_1109
